# v53: v52 variant - both 128-byte halves of each source row requested back to back (no load overlap across items within a wave)
# baseline (speedup 1.0000x reference)
; __device__ __forceinline__ unsigned pack_fp8x4(float a, float b, float c, float d) { int w = __builtin_amdgcn_cvt_pk_fp8_f32(a, b, 0, false); w = __builtin_amdgcn_cvt_pk_fp8_f32(c, d, w, true); return (unsigned)w; }
; #define LAS __attribute__((address_space(3)))
; __device__ __forceinline__ void mq_half_dma(const float* W, int N, int k0, int n0, LAS unsigned char* slice, int lane) {
;     const float* src = W + (size_t)(k0 + (lane >> 4)) * N + n0 + 4 * (lane & 15);
; #pragma unroll
;     for (int j = 0; j < 16; ++j) __builtin_amdgcn_global_load_lds((const unsigned*)(src + (size_t)(4 * j) * N), (LAS unsigned*)(slice + j * 1024), 16, 0, 2);
; }
; __device__ __forceinline__ void mq_half_cvt(unsigned char* WT, int dst_row0, int k0, const LAS unsigned char* slice, int lane) {
;     const int kq = lane >> 4, nq = lane & 15;
;     f32x4 v[16];
; #pragma unroll
;     for (int i = 0; i < 16; ++i) v[i] = *(const LAS f32x4*)(slice + (16 * kq + i) * 256 + nq * 16);
; #pragma unroll
;     for (int i = 0; i < 4; ++i) { v4u o;
;         o.x = pg8::pack_fp8x4(v[0][i] * 64.f, v[1][i] * 64.f, v[2][i] * 64.f, v[3][i] * 64.f); o.y = pg8::pack_fp8x4(v[4][i] * 64.f, v[5][i] * 64.f, v[6][i] * 64.f, v[7][i] * 64.f);
;         o.z = pg8::pack_fp8x4(v[8][i] * 64.f, v[9][i] * 64.f, v[10][i] * 64.f, v[11][i] * 64.f); o.w = pg8::pack_fp8x4(v[12][i] * 64.f, v[13][i] * 64.f, v[14][i] * 64.f, v[15][i] * 64.f);
;         __builtin_nontemporal_store(o, (v4u*)(WT + (size_t)(dst_row0 + 4 * nq + i) * 2048 + k0 + 16 * kq)); }
; __device__ __forceinline__ void moe_convert_queue(const Frame& F, const Args& A) {
;     ...
;             if (r < MQ_GU) { const int e = r / 1024, rr = r % 1024, kb = rr / 64, nb = rr % 64; const int pn = nb >> 2, q = nb & 3;
;                 W = A.in[I_WGU] + (size_t)e * 2048 * 4096; N = 4096; k0 = kb * 128 + 64 * kh; n0 = (q >> 1) * 2048 + 128 * pn + (q & 1) * 64; WT = (unsigned char*)(ws + WS_WGUT) + (size_t)e * 4096 * 2048; drow = nb * 64; }
.Lcq_ad0:
	s_mul_i32 s13, s38, s40
	s_add_i32 s13, s13, s12
	s_lshl_b32 s13, s13, 2
	s_add_u32 s10, s10, s13
	s_addc_u32 s11, s11, 0
	s_lshl_b32 s41, s40, 2
	v_mad_u32_u24 v8, v4, s41, v2
	s_lshl_b32 s13, s39, 11
	s_add_i32 s13, s13, s38
	s_add_u32 s24, s8, s13
	s_addc_u32 s25, s9, 0
	s_add_u32 s26, s24, 0x10000
	s_addc_u32 s27, s25, 0
	s_mov_b64 s[12:13], s[10:11]
	global_load_dwordx4 v[10:13], v8, s[10:11] nt
	s_add_u32 s10, s10, s41
	s_addc_u32 s11, s11, 0
	global_load_dwordx4 v[14:17], v8, s[10:11] nt
	s_add_u32 s10, s10, s41
	s_addc_u32 s11, s11, 0
	global_load_dwordx4 v[18:21], v8, s[10:11] nt
	s_add_u32 s10, s10, s41
	s_addc_u32 s11, s11, 0
	global_load_dwordx4 v[22:25], v8, s[10:11] nt
	s_add_u32 s10, s10, s41
	s_addc_u32 s11, s11, 0
	global_load_dwordx4 v[26:29], v8, s[10:11] nt
	s_add_u32 s10, s10, s41
	s_addc_u32 s11, s11, 0
	global_load_dwordx4 v[30:33], v8, s[10:11] nt
	s_add_u32 s10, s10, s41
	s_addc_u32 s11, s11, 0
	global_load_dwordx4 v[34:37], v8, s[10:11] nt
	s_add_u32 s10, s10, s41
	s_addc_u32 s11, s11, 0
	global_load_dwordx4 v[38:41], v8, s[10:11] nt
	s_add_u32 s10, s10, s41
	s_addc_u32 s11, s11, 0
	global_load_dwordx4 v[42:45], v8, s[10:11] nt
	s_add_u32 s10, s10, s41
	s_addc_u32 s11, s11, 0
	global_load_dwordx4 v[46:49], v8, s[10:11] nt
	s_add_u32 s10, s10, s41
	s_addc_u32 s11, s11, 0
	global_load_dwordx4 v[50:53], v8, s[10:11] nt
	s_add_u32 s10, s10, s41
	s_addc_u32 s11, s11, 0
	global_load_dwordx4 v[54:57], v8, s[10:11] nt
	s_add_u32 s10, s10, s41
	s_addc_u32 s11, s11, 0
	global_load_dwordx4 v[58:61], v8, s[10:11] nt
	s_add_u32 s10, s10, s41
	s_addc_u32 s11, s11, 0
	global_load_dwordx4 v[62:65], v8, s[10:11] nt
	s_add_u32 s10, s10, s41
	s_addc_u32 s11, s11, 0
	global_load_dwordx4 v[66:69], v8, s[10:11] nt
	s_add_u32 s10, s10, s41
	s_addc_u32 s11, s11, 0
	global_load_dwordx4 v[70:73], v8, s[10:11] nt
	global_load_dwordx4 v[100:103], v8, s[12:13] offset:128 nt
	s_add_u32 s12, s12, s41
	s_addc_u32 s13, s13, 0
	global_load_dwordx4 v[104:107], v8, s[12:13] offset:128 nt
	s_add_u32 s12, s12, s41
	s_addc_u32 s13, s13, 0
	global_load_dwordx4 v[108:111], v8, s[12:13] offset:128 nt
	s_add_u32 s12, s12, s41
	s_addc_u32 s13, s13, 0
	global_load_dwordx4 v[112:115], v8, s[12:13] offset:128 nt
	s_add_u32 s12, s12, s41
	s_addc_u32 s13, s13, 0
	global_load_dwordx4 v[116:119], v8, s[12:13] offset:128 nt
	s_add_u32 s12, s12, s41
	s_addc_u32 s13, s13, 0
	global_load_dwordx4 v[120:123], v8, s[12:13] offset:128 nt
	s_add_u32 s12, s12, s41
	s_addc_u32 s13, s13, 0
	global_load_dwordx4 v[124:127], v8, s[12:13] offset:128 nt
	s_add_u32 s12, s12, s41
	s_addc_u32 s13, s13, 0
	global_load_dwordx4 v[128:131], v8, s[12:13] offset:128 nt
	s_add_u32 s12, s12, s41
	s_addc_u32 s13, s13, 0
	global_load_dwordx4 v[132:135], v8, s[12:13] offset:128 nt
	s_add_u32 s12, s12, s41
	s_addc_u32 s13, s13, 0
	global_load_dwordx4 v[136:139], v8, s[12:13] offset:128 nt
	s_add_u32 s12, s12, s41
	s_addc_u32 s13, s13, 0
	global_load_dwordx4 v[140:143], v8, s[12:13] offset:128 nt
	s_add_u32 s12, s12, s41
	s_addc_u32 s13, s13, 0
	global_load_dwordx4 v[144:147], v8, s[12:13] offset:128 nt
	s_add_u32 s12, s12, s41
	s_addc_u32 s13, s13, 0
	global_load_dwordx4 v[148:151], v8, s[12:13] offset:128 nt
	s_add_u32 s12, s12, s41
	s_addc_u32 s13, s13, 0
	global_load_dwordx4 v[152:155], v8, s[12:13] offset:128 nt
	s_add_u32 s12, s12, s41
	s_addc_u32 s13, s13, 0
	global_load_dwordx4 v[156:159], v8, s[12:13] offset:128 nt
	s_add_u32 s12, s12, s41
	s_addc_u32 s13, s13, 0
	global_load_dwordx4 v[160:163], v8, s[12:13] offset:128 nt
	s_waitcnt vmcnt(16)
	v_pk_mul_f32 v[10:11], v[10:11], s[22:23] op_sel_hi:[1,0]
	v_pk_mul_f32 v[12:13], v[12:13], s[22:23] op_sel_hi:[1,0]
	v_pk_mul_f32 v[14:15], v[14:15], s[22:23] op_sel_hi:[1,0]
	v_pk_mul_f32 v[16:17], v[16:17], s[22:23] op_sel_hi:[1,0]
	v_pk_mul_f32 v[18:19], v[18:19], s[22:23] op_sel_hi:[1,0]
	v_pk_mul_f32 v[20:21], v[20:21], s[22:23] op_sel_hi:[1,0]
	v_pk_mul_f32 v[22:23], v[22:23], s[22:23] op_sel_hi:[1,0]
	v_pk_mul_f32 v[24:25], v[24:25], s[22:23] op_sel_hi:[1,0]
	v_pk_mul_f32 v[26:27], v[26:27], s[22:23] op_sel_hi:[1,0]
	v_pk_mul_f32 v[28:29], v[28:29], s[22:23] op_sel_hi:[1,0]
	v_pk_mul_f32 v[30:31], v[30:31], s[22:23] op_sel_hi:[1,0]
	v_pk_mul_f32 v[32:33], v[32:33], s[22:23] op_sel_hi:[1,0]
	v_pk_mul_f32 v[34:35], v[34:35], s[22:23] op_sel_hi:[1,0]
	v_pk_mul_f32 v[36:37], v[36:37], s[22:23] op_sel_hi:[1,0]
	v_pk_mul_f32 v[38:39], v[38:39], s[22:23] op_sel_hi:[1,0]
	v_pk_mul_f32 v[40:41], v[40:41], s[22:23] op_sel_hi:[1,0]
	v_pk_mul_f32 v[42:43], v[42:43], s[22:23] op_sel_hi:[1,0]
	v_pk_mul_f32 v[44:45], v[44:45], s[22:23] op_sel_hi:[1,0]
	v_pk_mul_f32 v[46:47], v[46:47], s[22:23] op_sel_hi:[1,0]
	v_pk_mul_f32 v[48:49], v[48:49], s[22:23] op_sel_hi:[1,0]
	v_pk_mul_f32 v[50:51], v[50:51], s[22:23] op_sel_hi:[1,0]
	v_pk_mul_f32 v[52:53], v[52:53], s[22:23] op_sel_hi:[1,0]
	v_pk_mul_f32 v[54:55], v[54:55], s[22:23] op_sel_hi:[1,0]
	v_pk_mul_f32 v[56:57], v[56:57], s[22:23] op_sel_hi:[1,0]
	v_pk_mul_f32 v[58:59], v[58:59], s[22:23] op_sel_hi:[1,0]
	v_pk_mul_f32 v[60:61], v[60:61], s[22:23] op_sel_hi:[1,0]
	v_pk_mul_f32 v[62:63], v[62:63], s[22:23] op_sel_hi:[1,0]
	v_pk_mul_f32 v[64:65], v[64:65], s[22:23] op_sel_hi:[1,0]
	v_pk_mul_f32 v[66:67], v[66:67], s[22:23] op_sel_hi:[1,0]
	v_pk_mul_f32 v[68:69], v[68:69], s[22:23] op_sel_hi:[1,0]
	v_pk_mul_f32 v[70:71], v[70:71], s[22:23] op_sel_hi:[1,0]
	v_pk_mul_f32 v[72:73], v[72:73], s[22:23] op_sel_hi:[1,0]
	v_cvt_pk_fp8_f32 v74, v10, v14
	v_cvt_pk_fp8_f32 v75, v26, v30
	v_cvt_pk_fp8_f32 v76, v42, v46
	v_cvt_pk_fp8_f32 v77, v58, v62
	v_cvt_pk_fp8_f32 v74, v18, v22 op_sel:[0,0,1]
	v_cvt_pk_fp8_f32 v75, v34, v38 op_sel:[0,0,1]
	v_cvt_pk_fp8_f32 v76, v50, v54 op_sel:[0,0,1]
	v_cvt_pk_fp8_f32 v77, v66, v70 op_sel:[0,0,1]
	v_cvt_pk_fp8_f32 v84, v11, v15
	v_cvt_pk_fp8_f32 v85, v27, v31
	v_cvt_pk_fp8_f32 v86, v43, v47
	v_cvt_pk_fp8_f32 v87, v59, v63
	v_cvt_pk_fp8_f32 v84, v19, v23 op_sel:[0,0,1]
	v_cvt_pk_fp8_f32 v85, v35, v39 op_sel:[0,0,1]
	v_cvt_pk_fp8_f32 v86, v51, v55 op_sel:[0,0,1]
	v_cvt_pk_fp8_f32 v87, v67, v71 op_sel:[0,0,1]
	global_store_dwordx4 v6, v[74:77], s[24:25] nt
	v_cvt_pk_fp8_f32 v88, v12, v16
	v_cvt_pk_fp8_f32 v89, v28, v32
	v_cvt_pk_fp8_f32 v90, v44, v48
	v_cvt_pk_fp8_f32 v91, v60, v64
	v_cvt_pk_fp8_f32 v88, v20, v24 op_sel:[0,0,1]
	v_cvt_pk_fp8_f32 v89, v36, v40 op_sel:[0,0,1]
	v_cvt_pk_fp8_f32 v90, v52, v56 op_sel:[0,0,1]
	v_cvt_pk_fp8_f32 v91, v68, v72 op_sel:[0,0,1]
	global_store_dwordx4 v6, v[84:87], s[24:25] offset:2048 nt
	v_cvt_pk_fp8_f32 v92, v13, v17
	v_cvt_pk_fp8_f32 v93, v29, v33
	v_cvt_pk_fp8_f32 v94, v45, v49
	v_cvt_pk_fp8_f32 v95, v61, v65
	v_cvt_pk_fp8_f32 v92, v21, v25 op_sel:[0,0,1]
	v_cvt_pk_fp8_f32 v93, v37, v41 op_sel:[0,0,1]
	v_cvt_pk_fp8_f32 v94, v53, v57 op_sel:[0,0,1]
	v_cvt_pk_fp8_f32 v95, v69, v73 op_sel:[0,0,1]
	global_store_dwordx4 v9, v[88:91], s[24:25] nt
	s_nop 1
	global_store_dwordx4 v9, v[92:95], s[24:25] offset:2048 nt
	s_waitcnt vmcnt(4)
; __device__ __forceinline__ unsigned pack_fp8x4(float a, float b, float c, float d) { int w = __builtin_amdgcn_cvt_pk_fp8_f32(a, b, 0, false); w = __builtin_amdgcn_cvt_pk_fp8_f32(c, d, w, true); return (unsigned)w; }
; __device__ __forceinline__ void mq_half_cvt(unsigned char* WT, int dst_row0, int k0, const LAS unsigned char* slice, int lane) {
;     ...
;     for (int i = 0; i < 4; ++i) { v4u o;
;         o.x = pg8::pack_fp8x4(v[0][i] * 64.f, v[1][i] * 64.f, v[2][i] * 64.f, v[3][i] * 64.f); o.y = pg8::pack_fp8x4(v[4][i] * 64.f, v[5][i] * 64.f, v[6][i] * 64.f, v[7][i] * 64.f);
;         o.z = pg8::pack_fp8x4(v[8][i] * 64.f, v[9][i] * 64.f, v[10][i] * 64.f, v[11][i] * 64.f); o.w = pg8::pack_fp8x4(v[12][i] * 64.f, v[13][i] * 64.f, v[14][i] * 64.f, v[15][i] * 64.f);
;         __builtin_nontemporal_store(o, (v4u*)(WT + (size_t)(dst_row0 + 4 * nq + i) * 2048 + k0 + 16 * kq)); }
; __device__ __forceinline__ void moe_convert_queue(const Frame& F, const Args& A) {
;     ...
;             if (r < MQ_GU) { const int e = r / 1024, rr = r % 1024, kb = rr / 64, nb = rr % 64; const int pn = nb >> 2, q = nb & 3;
;                 W = A.in[I_WGU] + (size_t)e * 2048 * 4096; N = 4096; k0 = kb * 128 + 64 * kh; n0 = (q >> 1) * 2048 + 128 * pn + (q & 1) * 64; WT = (unsigned char*)(ws + WS_WGUT) + (size_t)e * 4096 * 2048; drow = nb * 64; }
	v_pk_mul_f32 v[100:101], v[100:101], s[22:23] op_sel_hi:[1,0]
	v_pk_mul_f32 v[102:103], v[102:103], s[22:23] op_sel_hi:[1,0]
	v_pk_mul_f32 v[104:105], v[104:105], s[22:23] op_sel_hi:[1,0]
	v_pk_mul_f32 v[106:107], v[106:107], s[22:23] op_sel_hi:[1,0]
	v_pk_mul_f32 v[108:109], v[108:109], s[22:23] op_sel_hi:[1,0]
	v_pk_mul_f32 v[110:111], v[110:111], s[22:23] op_sel_hi:[1,0]
	v_pk_mul_f32 v[112:113], v[112:113], s[22:23] op_sel_hi:[1,0]
	v_pk_mul_f32 v[114:115], v[114:115], s[22:23] op_sel_hi:[1,0]
	v_pk_mul_f32 v[116:117], v[116:117], s[22:23] op_sel_hi:[1,0]
	v_pk_mul_f32 v[118:119], v[118:119], s[22:23] op_sel_hi:[1,0]
	v_pk_mul_f32 v[120:121], v[120:121], s[22:23] op_sel_hi:[1,0]
	v_pk_mul_f32 v[122:123], v[122:123], s[22:23] op_sel_hi:[1,0]
	v_pk_mul_f32 v[124:125], v[124:125], s[22:23] op_sel_hi:[1,0]
	v_pk_mul_f32 v[126:127], v[126:127], s[22:23] op_sel_hi:[1,0]
	v_pk_mul_f32 v[128:129], v[128:129], s[22:23] op_sel_hi:[1,0]
	v_pk_mul_f32 v[130:131], v[130:131], s[22:23] op_sel_hi:[1,0]
	v_pk_mul_f32 v[132:133], v[132:133], s[22:23] op_sel_hi:[1,0]
	v_pk_mul_f32 v[134:135], v[134:135], s[22:23] op_sel_hi:[1,0]
	v_pk_mul_f32 v[136:137], v[136:137], s[22:23] op_sel_hi:[1,0]
	v_pk_mul_f32 v[138:139], v[138:139], s[22:23] op_sel_hi:[1,0]
	v_pk_mul_f32 v[140:141], v[140:141], s[22:23] op_sel_hi:[1,0]
	v_pk_mul_f32 v[142:143], v[142:143], s[22:23] op_sel_hi:[1,0]
	v_pk_mul_f32 v[144:145], v[144:145], s[22:23] op_sel_hi:[1,0]
	v_pk_mul_f32 v[146:147], v[146:147], s[22:23] op_sel_hi:[1,0]
	v_pk_mul_f32 v[148:149], v[148:149], s[22:23] op_sel_hi:[1,0]
	v_pk_mul_f32 v[150:151], v[150:151], s[22:23] op_sel_hi:[1,0]
	v_pk_mul_f32 v[152:153], v[152:153], s[22:23] op_sel_hi:[1,0]
	v_pk_mul_f32 v[154:155], v[154:155], s[22:23] op_sel_hi:[1,0]
	v_pk_mul_f32 v[156:157], v[156:157], s[22:23] op_sel_hi:[1,0]
	v_pk_mul_f32 v[158:159], v[158:159], s[22:23] op_sel_hi:[1,0]
	v_pk_mul_f32 v[160:161], v[160:161], s[22:23] op_sel_hi:[1,0]
	v_pk_mul_f32 v[162:163], v[162:163], s[22:23] op_sel_hi:[1,0]
	v_cvt_pk_fp8_f32 v74, v100, v104
	v_cvt_pk_fp8_f32 v75, v116, v120
	v_cvt_pk_fp8_f32 v76, v132, v136
	v_cvt_pk_fp8_f32 v77, v148, v152
	v_cvt_pk_fp8_f32 v74, v108, v112 op_sel:[0,0,1]
	v_cvt_pk_fp8_f32 v75, v124, v128 op_sel:[0,0,1]
	v_cvt_pk_fp8_f32 v76, v140, v144 op_sel:[0,0,1]
	v_cvt_pk_fp8_f32 v77, v156, v160 op_sel:[0,0,1]
	v_cvt_pk_fp8_f32 v84, v101, v105
	v_cvt_pk_fp8_f32 v85, v117, v121
	v_cvt_pk_fp8_f32 v86, v133, v137
	v_cvt_pk_fp8_f32 v87, v149, v153
	v_cvt_pk_fp8_f32 v84, v109, v113 op_sel:[0,0,1]
	v_cvt_pk_fp8_f32 v85, v125, v129 op_sel:[0,0,1]
	v_cvt_pk_fp8_f32 v86, v141, v145 op_sel:[0,0,1]
	v_cvt_pk_fp8_f32 v87, v157, v161 op_sel:[0,0,1]
	global_store_dwordx4 v6, v[74:77], s[26:27] nt
	v_cvt_pk_fp8_f32 v88, v102, v106
	v_cvt_pk_fp8_f32 v89, v118, v122
	v_cvt_pk_fp8_f32 v90, v134, v138
	v_cvt_pk_fp8_f32 v91, v150, v154
	v_cvt_pk_fp8_f32 v88, v110, v114 op_sel:[0,0,1]
	v_cvt_pk_fp8_f32 v89, v126, v130 op_sel:[0,0,1]
	v_cvt_pk_fp8_f32 v90, v142, v146 op_sel:[0,0,1]
	v_cvt_pk_fp8_f32 v91, v158, v162 op_sel:[0,0,1]
	global_store_dwordx4 v6, v[84:87], s[26:27] offset:2048 nt
	v_cvt_pk_fp8_f32 v92, v103, v107
	v_cvt_pk_fp8_f32 v93, v119, v123
	v_cvt_pk_fp8_f32 v94, v135, v139
	v_cvt_pk_fp8_f32 v95, v151, v155
	v_cvt_pk_fp8_f32 v92, v111, v115 op_sel:[0,0,1]
	v_cvt_pk_fp8_f32 v93, v127, v131 op_sel:[0,0,1]
	v_cvt_pk_fp8_f32 v94, v143, v147 op_sel:[0,0,1]
	v_cvt_pk_fp8_f32 v95, v159, v163 op_sel:[0,0,1]
	global_store_dwordx4 v9, v[88:91], s[26:27] nt
	s_nop 1
	global_store_dwordx4 v9, v[92:95], s[26:27] offset:2048 nt
	s_add_i32 s42, s36, 1
	s_cmpk_gt_i32 s42, 0x7fff
	s_cbranch_scc1 .Lcq_dn2
	s_lshr_b32 s6, s42, 10
	s_and_b32 s8, s42, 0x3ff
	s_lshr_b32 s9, s8, 6
	s_and_b32 s8, s8, 63
	s_lshl_b32 s38, s9, 7
	s_lshl_b32 s39, s8, 6
	s_lshr_b32 s9, s8, 2
	s_lshl_b32 s9, s9, 7
	s_and_b32 s12, s8, 1
	s_lshl_b32 s12, s12, 6
	s_add_i32 s12, s12, s9
	s_and_b32 s9, s8, 2
	s_lshl_b32 s9, s9, 10
	s_add_i32 s12, s12, s9
	s_lshl_b64 s[10:11], s[6:7], 25
	s_add_u32 s10, s76, s10
	s_addc_u32 s11, s77, s11
	s_lshl_b64 s[8:9], s[6:7], 23
	s_add_u32 s8, s17, s8
	s_addc_u32 s9, s18, s9
	s_movk_i32 s40, 0x1000
	s_branch .Lcq_ad2

; __device__ __forceinline__ unsigned pack_fp8x4(float a, float b, float c, float d) { int w = __builtin_amdgcn_cvt_pk_fp8_f32(a, b, 0, false); w = __builtin_amdgcn_cvt_pk_fp8_f32(c, d, w, true); return (unsigned)w; }
; #define LAS __attribute__((address_space(3)))
; __device__ __forceinline__ void mq_half_dma(const float* W, int N, int k0, int n0, LAS unsigned char* slice, int lane) {
;     const float* src = W + (size_t)(k0 + (lane >> 4)) * N + n0 + 4 * (lane & 15);
; #pragma unroll
;     for (int j = 0; j < 16; ++j) __builtin_amdgcn_global_load_lds((const unsigned*)(src + (size_t)(4 * j) * N), (LAS unsigned*)(slice + j * 1024), 16, 0, 2);
; }
; __device__ __forceinline__ void mq_half_cvt(unsigned char* WT, int dst_row0, int k0, const LAS unsigned char* slice, int lane) {
;     const int kq = lane >> 4, nq = lane & 15;
;     f32x4 v[16];
; #pragma unroll
;     for (int i = 0; i < 16; ++i) v[i] = *(const LAS f32x4*)(slice + (16 * kq + i) * 256 + nq * 16);
; #pragma unroll
;     for (int i = 0; i < 4; ++i) { v4u o;
;         o.x = pg8::pack_fp8x4(v[0][i] * 64.f, v[1][i] * 64.f, v[2][i] * 64.f, v[3][i] * 64.f); o.y = pg8::pack_fp8x4(v[4][i] * 64.f, v[5][i] * 64.f, v[6][i] * 64.f, v[7][i] * 64.f);
;         o.z = pg8::pack_fp8x4(v[8][i] * 64.f, v[9][i] * 64.f, v[10][i] * 64.f, v[11][i] * 64.f); o.w = pg8::pack_fp8x4(v[12][i] * 64.f, v[13][i] * 64.f, v[14][i] * 64.f, v[15][i] * 64.f);
;         __builtin_nontemporal_store(o, (v4u*)(WT + (size_t)(dst_row0 + 4 * nq + i) * 2048 + k0 + 16 * kq)); }
.Lcq_ad2:
	s_mul_i32 s13, s38, s40
	s_add_i32 s13, s13, s12
	s_lshl_b32 s13, s13, 2
	s_add_u32 s10, s10, s13
	s_addc_u32 s11, s11, 0
	s_lshl_b32 s41, s40, 2
	v_mad_u32_u24 v8, v4, s41, v2
	s_lshl_b32 s13, s39, 11
	s_add_i32 s13, s13, s38
	s_add_u32 s24, s8, s13
	s_addc_u32 s25, s9, 0
	s_add_u32 s26, s24, 0x10000
	s_addc_u32 s27, s25, 0
	s_mov_b64 s[12:13], s[10:11]
	global_load_dwordx4 v[10:13], v8, s[10:11] nt
	s_add_u32 s10, s10, s41
	s_addc_u32 s11, s11, 0
	global_load_dwordx4 v[14:17], v8, s[10:11] nt
	s_add_u32 s10, s10, s41
	s_addc_u32 s11, s11, 0
	global_load_dwordx4 v[18:21], v8, s[10:11] nt
	s_add_u32 s10, s10, s41
	s_addc_u32 s11, s11, 0
	global_load_dwordx4 v[22:25], v8, s[10:11] nt
	s_add_u32 s10, s10, s41
	s_addc_u32 s11, s11, 0
	global_load_dwordx4 v[26:29], v8, s[10:11] nt
	s_add_u32 s10, s10, s41
	s_addc_u32 s11, s11, 0
	global_load_dwordx4 v[30:33], v8, s[10:11] nt
	s_add_u32 s10, s10, s41
	s_addc_u32 s11, s11, 0
	global_load_dwordx4 v[34:37], v8, s[10:11] nt
	s_add_u32 s10, s10, s41
	s_addc_u32 s11, s11, 0
	global_load_dwordx4 v[38:41], v8, s[10:11] nt
	s_add_u32 s10, s10, s41
	s_addc_u32 s11, s11, 0
	global_load_dwordx4 v[42:45], v8, s[10:11] nt
	s_add_u32 s10, s10, s41
	s_addc_u32 s11, s11, 0
	global_load_dwordx4 v[46:49], v8, s[10:11] nt
	s_add_u32 s10, s10, s41
	s_addc_u32 s11, s11, 0
	global_load_dwordx4 v[50:53], v8, s[10:11] nt
	s_add_u32 s10, s10, s41
	s_addc_u32 s11, s11, 0
	global_load_dwordx4 v[54:57], v8, s[10:11] nt
	s_add_u32 s10, s10, s41
	s_addc_u32 s11, s11, 0
	global_load_dwordx4 v[58:61], v8, s[10:11] nt
	s_add_u32 s10, s10, s41
	s_addc_u32 s11, s11, 0
	global_load_dwordx4 v[62:65], v8, s[10:11] nt
	s_add_u32 s10, s10, s41
	s_addc_u32 s11, s11, 0
	global_load_dwordx4 v[66:69], v8, s[10:11] nt
	s_add_u32 s10, s10, s41
	s_addc_u32 s11, s11, 0
	global_load_dwordx4 v[70:73], v8, s[10:11] nt
	global_load_dwordx4 v[100:103], v8, s[12:13] offset:128 nt
	s_add_u32 s12, s12, s41
	s_addc_u32 s13, s13, 0
	global_load_dwordx4 v[104:107], v8, s[12:13] offset:128 nt
	s_add_u32 s12, s12, s41
	s_addc_u32 s13, s13, 0
	global_load_dwordx4 v[108:111], v8, s[12:13] offset:128 nt
	s_add_u32 s12, s12, s41
	s_addc_u32 s13, s13, 0
	global_load_dwordx4 v[112:115], v8, s[12:13] offset:128 nt
	s_add_u32 s12, s12, s41
	s_addc_u32 s13, s13, 0
	global_load_dwordx4 v[116:119], v8, s[12:13] offset:128 nt
	s_add_u32 s12, s12, s41
	s_addc_u32 s13, s13, 0
	global_load_dwordx4 v[120:123], v8, s[12:13] offset:128 nt
	s_add_u32 s12, s12, s41
	s_addc_u32 s13, s13, 0
	global_load_dwordx4 v[124:127], v8, s[12:13] offset:128 nt
	s_add_u32 s12, s12, s41
	s_addc_u32 s13, s13, 0
	global_load_dwordx4 v[128:131], v8, s[12:13] offset:128 nt
	s_add_u32 s12, s12, s41
	s_addc_u32 s13, s13, 0
	global_load_dwordx4 v[132:135], v8, s[12:13] offset:128 nt
	s_add_u32 s12, s12, s41
	s_addc_u32 s13, s13, 0
	global_load_dwordx4 v[136:139], v8, s[12:13] offset:128 nt
	s_add_u32 s12, s12, s41
	s_addc_u32 s13, s13, 0
	global_load_dwordx4 v[140:143], v8, s[12:13] offset:128 nt
	s_add_u32 s12, s12, s41
	s_addc_u32 s13, s13, 0
	global_load_dwordx4 v[144:147], v8, s[12:13] offset:128 nt
	s_add_u32 s12, s12, s41
	s_addc_u32 s13, s13, 0
	global_load_dwordx4 v[148:151], v8, s[12:13] offset:128 nt
	s_add_u32 s12, s12, s41
	s_addc_u32 s13, s13, 0
	global_load_dwordx4 v[152:155], v8, s[12:13] offset:128 nt
	s_add_u32 s12, s12, s41
	s_addc_u32 s13, s13, 0
	global_load_dwordx4 v[156:159], v8, s[12:13] offset:128 nt
	s_add_u32 s12, s12, s41
	s_addc_u32 s13, s13, 0
	global_load_dwordx4 v[160:163], v8, s[12:13] offset:128 nt
	s_waitcnt vmcnt(16)
	v_pk_mul_f32 v[10:11], v[10:11], s[22:23] op_sel_hi:[1,0]
	v_pk_mul_f32 v[12:13], v[12:13], s[22:23] op_sel_hi:[1,0]
	v_pk_mul_f32 v[14:15], v[14:15], s[22:23] op_sel_hi:[1,0]
	v_pk_mul_f32 v[16:17], v[16:17], s[22:23] op_sel_hi:[1,0]
	v_pk_mul_f32 v[18:19], v[18:19], s[22:23] op_sel_hi:[1,0]
	v_pk_mul_f32 v[20:21], v[20:21], s[22:23] op_sel_hi:[1,0]
	v_pk_mul_f32 v[22:23], v[22:23], s[22:23] op_sel_hi:[1,0]
	v_pk_mul_f32 v[24:25], v[24:25], s[22:23] op_sel_hi:[1,0]
	v_pk_mul_f32 v[26:27], v[26:27], s[22:23] op_sel_hi:[1,0]
	v_pk_mul_f32 v[28:29], v[28:29], s[22:23] op_sel_hi:[1,0]
	v_pk_mul_f32 v[30:31], v[30:31], s[22:23] op_sel_hi:[1,0]
	v_pk_mul_f32 v[32:33], v[32:33], s[22:23] op_sel_hi:[1,0]
	v_pk_mul_f32 v[34:35], v[34:35], s[22:23] op_sel_hi:[1,0]
	v_pk_mul_f32 v[36:37], v[36:37], s[22:23] op_sel_hi:[1,0]
	v_pk_mul_f32 v[38:39], v[38:39], s[22:23] op_sel_hi:[1,0]
	v_pk_mul_f32 v[40:41], v[40:41], s[22:23] op_sel_hi:[1,0]
	v_pk_mul_f32 v[42:43], v[42:43], s[22:23] op_sel_hi:[1,0]
	v_pk_mul_f32 v[44:45], v[44:45], s[22:23] op_sel_hi:[1,0]
	v_pk_mul_f32 v[46:47], v[46:47], s[22:23] op_sel_hi:[1,0]
	v_pk_mul_f32 v[48:49], v[48:49], s[22:23] op_sel_hi:[1,0]
	v_pk_mul_f32 v[50:51], v[50:51], s[22:23] op_sel_hi:[1,0]
	v_pk_mul_f32 v[52:53], v[52:53], s[22:23] op_sel_hi:[1,0]
	v_pk_mul_f32 v[54:55], v[54:55], s[22:23] op_sel_hi:[1,0]
	v_pk_mul_f32 v[56:57], v[56:57], s[22:23] op_sel_hi:[1,0]
	v_pk_mul_f32 v[58:59], v[58:59], s[22:23] op_sel_hi:[1,0]
	v_pk_mul_f32 v[60:61], v[60:61], s[22:23] op_sel_hi:[1,0]
	v_pk_mul_f32 v[62:63], v[62:63], s[22:23] op_sel_hi:[1,0]
	v_pk_mul_f32 v[64:65], v[64:65], s[22:23] op_sel_hi:[1,0]
	v_pk_mul_f32 v[66:67], v[66:67], s[22:23] op_sel_hi:[1,0]
	v_pk_mul_f32 v[68:69], v[68:69], s[22:23] op_sel_hi:[1,0]
	v_pk_mul_f32 v[70:71], v[70:71], s[22:23] op_sel_hi:[1,0]
	v_pk_mul_f32 v[72:73], v[72:73], s[22:23] op_sel_hi:[1,0]
	v_cvt_pk_fp8_f32 v74, v10, v14
	v_cvt_pk_fp8_f32 v75, v26, v30
	v_cvt_pk_fp8_f32 v76, v42, v46
	v_cvt_pk_fp8_f32 v77, v58, v62
	v_cvt_pk_fp8_f32 v74, v18, v22 op_sel:[0,0,1]
	v_cvt_pk_fp8_f32 v75, v34, v38 op_sel:[0,0,1]
	v_cvt_pk_fp8_f32 v76, v50, v54 op_sel:[0,0,1]
	v_cvt_pk_fp8_f32 v77, v66, v70 op_sel:[0,0,1]
	v_cvt_pk_fp8_f32 v84, v11, v15
	v_cvt_pk_fp8_f32 v85, v27, v31
	v_cvt_pk_fp8_f32 v86, v43, v47
	v_cvt_pk_fp8_f32 v87, v59, v63
	v_cvt_pk_fp8_f32 v84, v19, v23 op_sel:[0,0,1]
	v_cvt_pk_fp8_f32 v85, v35, v39 op_sel:[0,0,1]
	v_cvt_pk_fp8_f32 v86, v51, v55 op_sel:[0,0,1]
	v_cvt_pk_fp8_f32 v87, v67, v71 op_sel:[0,0,1]
	global_store_dwordx4 v6, v[74:77], s[24:25] nt
	v_cvt_pk_fp8_f32 v88, v12, v16
	v_cvt_pk_fp8_f32 v89, v28, v32
	v_cvt_pk_fp8_f32 v90, v44, v48
	v_cvt_pk_fp8_f32 v91, v60, v64
	v_cvt_pk_fp8_f32 v88, v20, v24 op_sel:[0,0,1]
	v_cvt_pk_fp8_f32 v89, v36, v40 op_sel:[0,0,1]
	v_cvt_pk_fp8_f32 v90, v52, v56 op_sel:[0,0,1]
	v_cvt_pk_fp8_f32 v91, v68, v72 op_sel:[0,0,1]
	global_store_dwordx4 v6, v[84:87], s[24:25] offset:2048 nt
	v_cvt_pk_fp8_f32 v92, v13, v17
	v_cvt_pk_fp8_f32 v93, v29, v33
	v_cvt_pk_fp8_f32 v94, v45, v49
	v_cvt_pk_fp8_f32 v95, v61, v65
	v_cvt_pk_fp8_f32 v92, v21, v25 op_sel:[0,0,1]
	v_cvt_pk_fp8_f32 v93, v37, v41 op_sel:[0,0,1]
	v_cvt_pk_fp8_f32 v94, v53, v57 op_sel:[0,0,1]
	v_cvt_pk_fp8_f32 v95, v69, v73 op_sel:[0,0,1]
	global_store_dwordx4 v9, v[88:91], s[24:25] nt
	s_nop 1
	global_store_dwordx4 v9, v[92:95], s[24:25] offset:2048 nt
	s_waitcnt vmcnt(4)
; __device__ __forceinline__ unsigned pack_fp8x4(float a, float b, float c, float d) { int w = __builtin_amdgcn_cvt_pk_fp8_f32(a, b, 0, false); w = __builtin_amdgcn_cvt_pk_fp8_f32(c, d, w, true); return (unsigned)w; }
; __device__ __forceinline__ void mq_half_cvt(unsigned char* WT, int dst_row0, int k0, const LAS unsigned char* slice, int lane) {
;     ...
;     for (int i = 0; i < 4; ++i) { v4u o;
;         o.x = pg8::pack_fp8x4(v[0][i] * 64.f, v[1][i] * 64.f, v[2][i] * 64.f, v[3][i] * 64.f); o.y = pg8::pack_fp8x4(v[4][i] * 64.f, v[5][i] * 64.f, v[6][i] * 64.f, v[7][i] * 64.f);
;         o.z = pg8::pack_fp8x4(v[8][i] * 64.f, v[9][i] * 64.f, v[10][i] * 64.f, v[11][i] * 64.f); o.w = pg8::pack_fp8x4(v[12][i] * 64.f, v[13][i] * 64.f, v[14][i] * 64.f, v[15][i] * 64.f);
;         __builtin_nontemporal_store(o, (v4u*)(WT + (size_t)(dst_row0 + 4 * nq + i) * 2048 + k0 + 16 * kq)); }
	v_pk_mul_f32 v[100:101], v[100:101], s[22:23] op_sel_hi:[1,0]
	v_pk_mul_f32 v[102:103], v[102:103], s[22:23] op_sel_hi:[1,0]
	v_pk_mul_f32 v[104:105], v[104:105], s[22:23] op_sel_hi:[1,0]
	v_pk_mul_f32 v[106:107], v[106:107], s[22:23] op_sel_hi:[1,0]
	v_pk_mul_f32 v[108:109], v[108:109], s[22:23] op_sel_hi:[1,0]
	v_pk_mul_f32 v[110:111], v[110:111], s[22:23] op_sel_hi:[1,0]
	v_pk_mul_f32 v[112:113], v[112:113], s[22:23] op_sel_hi:[1,0]
	v_pk_mul_f32 v[114:115], v[114:115], s[22:23] op_sel_hi:[1,0]
	v_pk_mul_f32 v[116:117], v[116:117], s[22:23] op_sel_hi:[1,0]
	v_pk_mul_f32 v[118:119], v[118:119], s[22:23] op_sel_hi:[1,0]
	v_pk_mul_f32 v[120:121], v[120:121], s[22:23] op_sel_hi:[1,0]
	v_pk_mul_f32 v[122:123], v[122:123], s[22:23] op_sel_hi:[1,0]
	v_pk_mul_f32 v[124:125], v[124:125], s[22:23] op_sel_hi:[1,0]
	v_pk_mul_f32 v[126:127], v[126:127], s[22:23] op_sel_hi:[1,0]
	v_pk_mul_f32 v[128:129], v[128:129], s[22:23] op_sel_hi:[1,0]
	v_pk_mul_f32 v[130:131], v[130:131], s[22:23] op_sel_hi:[1,0]
	v_pk_mul_f32 v[132:133], v[132:133], s[22:23] op_sel_hi:[1,0]
	v_pk_mul_f32 v[134:135], v[134:135], s[22:23] op_sel_hi:[1,0]
	v_pk_mul_f32 v[136:137], v[136:137], s[22:23] op_sel_hi:[1,0]
	v_pk_mul_f32 v[138:139], v[138:139], s[22:23] op_sel_hi:[1,0]
	v_pk_mul_f32 v[140:141], v[140:141], s[22:23] op_sel_hi:[1,0]
	v_pk_mul_f32 v[142:143], v[142:143], s[22:23] op_sel_hi:[1,0]
	v_pk_mul_f32 v[144:145], v[144:145], s[22:23] op_sel_hi:[1,0]
	v_pk_mul_f32 v[146:147], v[146:147], s[22:23] op_sel_hi:[1,0]
	v_pk_mul_f32 v[148:149], v[148:149], s[22:23] op_sel_hi:[1,0]
	v_pk_mul_f32 v[150:151], v[150:151], s[22:23] op_sel_hi:[1,0]
	v_pk_mul_f32 v[152:153], v[152:153], s[22:23] op_sel_hi:[1,0]
	v_pk_mul_f32 v[154:155], v[154:155], s[22:23] op_sel_hi:[1,0]
	v_pk_mul_f32 v[156:157], v[156:157], s[22:23] op_sel_hi:[1,0]
	v_pk_mul_f32 v[158:159], v[158:159], s[22:23] op_sel_hi:[1,0]
	v_pk_mul_f32 v[160:161], v[160:161], s[22:23] op_sel_hi:[1,0]
	v_pk_mul_f32 v[162:163], v[162:163], s[22:23] op_sel_hi:[1,0]
	v_cvt_pk_fp8_f32 v74, v100, v104
	v_cvt_pk_fp8_f32 v75, v116, v120
	v_cvt_pk_fp8_f32 v76, v132, v136
	v_cvt_pk_fp8_f32 v77, v148, v152
	v_cvt_pk_fp8_f32 v74, v108, v112 op_sel:[0,0,1]
	v_cvt_pk_fp8_f32 v75, v124, v128 op_sel:[0,0,1]
	v_cvt_pk_fp8_f32 v76, v140, v144 op_sel:[0,0,1]
	v_cvt_pk_fp8_f32 v77, v156, v160 op_sel:[0,0,1]
	v_cvt_pk_fp8_f32 v84, v101, v105
	v_cvt_pk_fp8_f32 v85, v117, v121
	v_cvt_pk_fp8_f32 v86, v133, v137
	v_cvt_pk_fp8_f32 v87, v149, v153
	v_cvt_pk_fp8_f32 v84, v109, v113 op_sel:[0,0,1]
	v_cvt_pk_fp8_f32 v85, v125, v129 op_sel:[0,0,1]
	v_cvt_pk_fp8_f32 v86, v141, v145 op_sel:[0,0,1]
	v_cvt_pk_fp8_f32 v87, v157, v161 op_sel:[0,0,1]
	global_store_dwordx4 v6, v[74:77], s[26:27] nt
	v_cvt_pk_fp8_f32 v88, v102, v106
	v_cvt_pk_fp8_f32 v89, v118, v122
	v_cvt_pk_fp8_f32 v90, v134, v138
	v_cvt_pk_fp8_f32 v91, v150, v154
	v_cvt_pk_fp8_f32 v88, v110, v114 op_sel:[0,0,1]
	v_cvt_pk_fp8_f32 v89, v126, v130 op_sel:[0,0,1]
	v_cvt_pk_fp8_f32 v90, v142, v146 op_sel:[0,0,1]
	v_cvt_pk_fp8_f32 v91, v158, v162 op_sel:[0,0,1]
	global_store_dwordx4 v6, v[84:87], s[26:27] offset:2048 nt
	v_cvt_pk_fp8_f32 v92, v103, v107
	v_cvt_pk_fp8_f32 v93, v119, v123
	v_cvt_pk_fp8_f32 v94, v135, v139
	v_cvt_pk_fp8_f32 v95, v151, v155
	v_cvt_pk_fp8_f32 v92, v111, v115 op_sel:[0,0,1]
	v_cvt_pk_fp8_f32 v93, v127, v131 op_sel:[0,0,1]
	v_cvt_pk_fp8_f32 v94, v143, v147 op_sel:[0,0,1]
	v_cvt_pk_fp8_f32 v95, v159, v163 op_sel:[0,0,1]
	global_store_dwordx4 v9, v[88:91], s[26:27] nt
	s_nop 1
	global_store_dwordx4 v9, v[92:95], s[26:27] offset:2048 nt
	s_branch .Lcq_grab
